# v069 + poll-loop tightening: the non-last XCD leaders spin on the TOP counter without s_sleep between polls at the 9 in-loop barrier sites
# speedup vs baseline: 1.0070x; 1.0070x over previous
; __device__ __forceinline__ unsigned xb_ld(unsigned* p)              { return __hip_atomic_load(p, __ATOMIC_RELAXED, __HIP_MEMORY_SCOPE_AGENT); }
; __device__ __forceinline__ unsigned xb_add(unsigned* p, unsigned v) { return __hip_atomic_fetch_add(p, v, __ATOMIC_RELAXED, __HIP_MEMORY_SCOPE_AGENT); }
; #define XB_SPIN(cond, bar) do { unsigned _sp = 0; while (cond) { __builtin_amdgcn_s_sleep(1); \
;     if ((++_sp & 255u) == 0u) { if (xb_ld(&(bar)[XB_TMO])) break; if (_sp > XB_SPIN_CAP) { atomicAdd(&(bar)[XB_TMO], 1u); break; } } } } while (0)
; __device__ __forceinline__ void xcd_barrier(const XcdBarrier& b, const int tid) {
;     ...
;             const unsigned og = xb_add(&bar[XB_TOP], 1u);
;             const unsigned tg = og / nx;
;             if (og + 1u == (tg + 1u) * nx) xb_add(&bar[XB_TOPGEN], 1u);
;             else XB_SPIN(xb_ld(&bar[XB_TOPGEN]) == tg, bar);
.LBB0_751:
	s_and_b32 s11, s7, 0xff
	s_mov_b64 s[48:49], -1
	s_cmp_lg_u32 s11, 0
	s_mov_b64 s[58:59], -1
	s_nop 0
	s_cbranch_scc1 .LBB0_754
	v_readlane_b32 s22, v251, 7
	v_readlane_b32 s23, v251, 8
	s_nop 4
	global_load_dword v2, v1, s[22:23] sc1
	s_waitcnt vmcnt(0)
	v_cmp_eq_u32_e32 vcc, 0, v2
	s_cbranch_vccnz .LBB0_756
	s_mov_b64 s[58:59], 0
	s_mov_b64 s[54:55], -1

; __device__ __forceinline__ unsigned xb_ld(unsigned* p)              { return __hip_atomic_load(p, __ATOMIC_RELAXED, __HIP_MEMORY_SCOPE_AGENT); }
; __device__ __forceinline__ unsigned xb_add(unsigned* p, unsigned v) { return __hip_atomic_fetch_add(p, v, __ATOMIC_RELAXED, __HIP_MEMORY_SCOPE_AGENT); }
; #define XB_SPIN(cond, bar) do { unsigned _sp = 0; while (cond) { __builtin_amdgcn_s_sleep(1); \
;     if ((++_sp & 255u) == 0u) { if (xb_ld(&(bar)[XB_TMO])) break; if (_sp > XB_SPIN_CAP) { atomicAdd(&(bar)[XB_TMO], 1u); break; } } } } while (0)
; __device__ __forceinline__ void xcd_barrier(const XcdBarrier& b, const int tid) {
;     ...
;             const unsigned og = xb_add(&bar[XB_TOP], 1u);
;             const unsigned tg = og / nx;
;             if (og + 1u == (tg + 1u) * nx) xb_add(&bar[XB_TOPGEN], 1u);
;             else XB_SPIN(xb_ld(&bar[XB_TOPGEN]) == tg, bar);
.LBB0_1823:
	s_and_b32 s7, s6, 0xff
	s_mov_b64 s[48:49], -1
	s_cmp_lg_u32 s7, 0
	s_mov_b64 s[58:59], -1
	s_nop 0
	s_cbranch_scc1 .LBB0_1826
	v_readlane_b32 s22, v251, 7
	v_readlane_b32 s23, v251, 8
	s_nop 4
	global_load_dword v2, v1, s[22:23] sc1
	s_waitcnt vmcnt(0)
	v_cmp_eq_u32_e32 vcc, 0, v2
	s_cbranch_vccnz .LBB0_1828
	s_mov_b64 s[58:59], 0
	s_mov_b64 s[54:55], -1
